# P2 attention: K/V rows staged by LDS-DMA (source-side swizzle), q fragments requested before the staging barrier; on top of the ring-ahead LDS reads
# baseline (speedup 1.0000x reference)
.LBB0_239:
	v_writelane_b32 v242, s80, 10
	s_cmp_lt_i32 s44, 3
	s_cselect_b64 s[0:1], -1, 0
	v_writelane_b32 v242, s81, 11
	v_writelane_b32 v242, s82, 12
	v_writelane_b32 v242, s83, 13
	v_writelane_b32 v242, s84, 14
	s_and_b64 s[0:1], s[0:1], s[4:5]
	v_writelane_b32 v242, s85, 15
	s_andn2_b64 vcc, exec, s[0:1]
	v_writelane_b32 v242, s86, 16
	v_writelane_b32 v242, s87, 17
	s_cbranch_vccnz .LBB0_246
	s_cmpk_gt_i32 s94, 0x11ff
	s_cbranch_scc1 .LBB0_246
	s_add_u32 s3, s46, 0x8e00000
	s_addc_u32 s33, s47, 0
	s_add_u32 s22, s46, 0x12e00000
	s_addc_u32 s23, s47, 0
	v_readlane_b32 s4, v242, 6
	s_add_u32 s24, s46, 0x100000
	v_lshrrev_b32_e32 v3, 4, v146
	s_mov_b32 s6, s4
	s_addc_u32 s25, s47, 0
	v_and_b32_e32 v5, 15, v0
	s_lshl_b32 s4, s4, 4
	s_waitcnt vmcnt(0)
	v_lshlrev_b32_e32 v6, 2, v3
	v_bfe_u32 v9, v0, 2, 2
	s_lshl_b32 s6, s6, 12
	v_lshlrev_b32_e32 v7, 3, v0
	v_sub_u32_e32 v8, v5, v6
	v_or3_b32 v9, s4, v9, v6
	v_lshrrev_b32_e32 v13, 3, v0
	s_add_i32 s6, s6, 0
	v_or_b32_e32 v58, s4, v5
	v_and_b32_e32 v2, 0x78, v7
	v_lshlrev_b32_e32 v4, 3, v3
	v_and_b32_e32 v7, 8, v7
	s_add_i32 s44, 0, 0x10000
	v_bitop3_b32 v13, v13, v5, 14 bitop3:0x6c
	v_bitop3_b32 v32, v3, v0, 15 bitop3:0x78
	v_lshl_add_u32 v33, v5, 8, s6
	v_bitop3_b32 v34, v3, v5, 4 bitop3:0x36
	v_bitop3_b32 v35, v3, v5, 8 bitop3:0x36
	v_bitop3_b32 v3, v3, v5, 12 bitop3:0x36
	v_cmp_gt_i32_e64 s[6:7], 1, v8
	v_cmp_gt_i32_e64 s[8:9], 2, v8
	v_cmp_gt_i32_e64 s[10:11], 3, v8
	v_cmp_gt_i32_e64 s[12:13], 4, v8
	v_cmp_lt_i32_e64 s[14:15], -1, v8
	v_cmp_lt_i32_e64 s[16:17], 0, v8
	v_cmp_lt_i32_e64 s[18:19], 1, v8
	v_cmp_lt_i32_e64 s[20:21], 2, v8
	v_lshlrev_b32_e32 v5, 8, v9
	v_lshlrev_b32_e32 v8, 1, v9
	v_and_b32_e32 v9, 14, v8
	v_add3_u32 v67, s44, v7, v5
	v_add3_u32 v68, s44, v5, v7
	v_bfe_u32 v5, v0, 1, 1
	v_or_b32_e32 v7, v9, v5
	v_lshlrev_b32_e32 v69, 4, v7
	v_or_b32_e32 v7, 2, v5
	v_bitop3_b32 v7, v8, v7, 14 bitop3:0x6c
	v_lshlrev_b32_e32 v70, 4, v7
	v_or_b32_e32 v7, 4, v5
	v_bitop3_b32 v7, v8, v7, 14 bitop3:0x6c
	v_or_b32_e32 v10, 0x200, v0
	s_cmpk_gt_u32 s96, 0x1ff
	v_lshlrev_b32_e32 v71, 4, v7
	v_or_b32_e32 v7, 6, v5
	v_lshrrev_b32_e32 v60, 4, v10
	v_or_b32_e32 v10, 0x600, v0
	s_cselect_b64 s[26:27], -1, 0
	s_cmpk_gt_u32 s96, 0x1bf
	v_bitop3_b32 v7, v8, v7, 14 bitop3:0x6c
	v_lshrrev_b32_e32 v62, 4, v10
	v_or_b32_e32 v10, 0xa00, v0
	s_cselect_b64 s[28:29], -1, 0
	s_cmpk_gt_u32 s96, 0x17f
	v_lshlrev_b32_e32 v72, 4, v7
	v_or_b32_e32 v7, 8, v5
	v_lshrrev_b32_e32 v64, 4, v10
	v_or_b32_e32 v10, 0xe00, v0
	s_cselect_b64 s[30:31], -1, 0
	s_cmpk_gt_u32 s96, 0x13f
	v_bitop3_b32 v7, v8, v7, 14 bitop3:0x6c
	v_lshrrev_b32_e32 v59, 4, v0
	v_lshrrev_b32_e32 v66, 4, v10
	s_cselect_b64 s[34:35], -1, 0
	s_cmpk_gt_u32 s96, 0xff
	v_lshlrev_b32_e32 v73, 4, v7
	v_or_b32_e32 v7, 10, v5
	v_or_b32_e32 v61, 64, v59
	v_or_b32_e32 v63, 0x80, v59
	v_or_b32_e32 v65, 0xc0, v59
	v_xor_b32_e32 v12, v59, v0
	v_xor_b32_e32 v16, v60, v0
	v_xor_b32_e32 v21, v62, v0
	v_xor_b32_e32 v26, v64, v0
	v_xor_b32_e32 v31, v66, v0
	s_cselect_b64 s[36:37], -1, 0
	s_cmpk_gt_u32 s96, 0xbf
	v_bitop3_b32 v7, v8, v7, 14 bitop3:0x6c
	v_lshlrev_b32_e32 v10, 8, v59
	v_lshlrev_b32_e32 v12, 4, v12
	v_lshlrev_b32_e32 v14, 8, v60
	v_lshlrev_b32_e32 v16, 4, v16
	v_lshlrev_b32_e32 v17, 8, v61
	v_lshlrev_b32_e32 v19, 8, v62
	v_lshlrev_b32_e32 v21, 4, v21
	v_lshlrev_b32_e32 v22, 8, v63
	v_lshlrev_b32_e32 v24, 8, v64
	v_lshlrev_b32_e32 v26, 4, v26
	v_lshlrev_b32_e32 v27, 8, v65
	v_lshlrev_b32_e32 v29, 8, v66
	v_lshlrev_b32_e32 v31, 4, v31
	s_cselect_b64 s[38:39], -1, 0
	s_cmpk_gt_u32 s96, 0x7f
	v_lshlrev_b32_e32 v74, 4, v7
	v_or_b32_e32 v7, 12, v5
	v_readlane_b32 s5, v242, 7
	v_add_u32_e32 v11, 0, v10
	v_and_b32_e32 v12, 0xf0, v12
	v_add_u32_e32 v10, s44, v10
	v_lshlrev_b32_e32 v13, 4, v13
	v_add_u32_e32 v15, 0, v14
	v_and_b32_e32 v16, 0xf0, v16
	v_add_u32_e32 v14, s44, v14
	v_add_u32_e32 v18, 0, v17
	v_add_u32_e32 v17, s44, v17
	v_add_u32_e32 v20, 0, v19
	v_and_b32_e32 v21, 0xf0, v21
	v_add_u32_e32 v19, s44, v19
	v_add_u32_e32 v23, 0, v22
	v_add_u32_e32 v22, s44, v22
	v_add_u32_e32 v25, 0, v24
	v_and_b32_e32 v26, 0xf0, v26
	v_add_u32_e32 v24, s44, v24
	v_add_u32_e32 v28, 0, v27
	v_add_u32_e32 v27, s44, v27
	v_add_u32_e32 v30, 0, v29
	v_and_b32_e32 v31, 0xf0, v31
	v_add_u32_e32 v29, s44, v29
	v_lshlrev_b32_e32 v32, 4, v32
	v_lshlrev_b32_e32 v34, 4, v34
	v_lshlrev_b32_e32 v35, 4, v35
	v_lshlrev_b32_e32 v3, 4, v3
	s_cselect_b64 s[40:41], -1, 0
	s_cmp_gt_u32 s96, 63
	v_bitop3_b32 v7, v8, v7, 14 bitop3:0x6c
	v_bitop3_b32 v5, v8, v5, 14 bitop3:0x4e
	v_lshlrev_b32_e32 v52, 1, v2
	v_mbcnt_lo_u32_b32 v2, -1, 0
	v_mov_b32_e32 v51, 0
	v_cmp_gt_u32_e64 s[4:5], 16, v146
	s_cselect_b64 s[42:43], -1, 0
	v_lshlrev_b32_e32 v75, 4, v7
	v_lshlrev_b32_e32 v76, 4, v5
	v_add_u32_e32 v77, 0x2000, v67
	v_add_u32_e32 v78, 0x4000, v67
	v_add_u32_e32 v79, 0x6000, v67
	s_movk_i32 s44, 0x1000
	v_add_u32_e32 v80, v11, v12
	v_add_u32_e32 v81, v10, v13
	v_add_u32_e32 v82, v15, v16
	v_add_u32_e32 v83, v14, v13
	v_add_u32_e32 v84, v18, v12
	v_add_u32_e32 v85, v17, v13
	v_add_u32_e32 v86, v20, v21
	v_add_u32_e32 v87, v19, v13
	v_add_u32_e32 v88, v23, v12
	v_add_u32_e32 v89, v22, v13
	v_add_u32_e32 v90, v25, v26
	v_add_u32_e32 v91, v24, v13
	v_add_u32_e32 v92, v28, v12
	v_add_u32_e32 v93, v27, v13
	v_add_u32_e32 v94, v30, v31
	v_add_u32_e32 v95, v29, v13
	v_add_u32_e32 v140, 0xc00, v12
	v_mov_b32_e32 v141, 0
	v_sub_u32_e32 v144, v13, v12
	v_add_u32_e32 v144, 0xc00, v144
	v_readlane_b32 s86, v242, 6
	s_nop 3
	s_lshl_b32 s86, s86, 10
	s_add_i32 s87, s86, 0x10000
	v_lshlrev_b32_e32 v54, 1, v4
	v_add_u32_e32 v96, v33, v32
	v_add_u32_e32 v97, v33, v34
	v_add_u32_e32 v98, v33, v35
	v_add_u32_e32 v99, v33, v3
	v_mbcnt_hi_u32_b32 v100, -1, v2
	s_mov_b32 s54, 0x3e0293ee
	s_movk_i32 s45, 0xc00
	v_lshlrev_b32_e32 v56, 1, v6
	v_mov_b32_e32 v101, 0xff800000
	v_mov_b32_e32 v102, 0x41b17218
	s_mov_b32 s55, s94
	s_branch .LBB0_243

.LBB0_243:
	s_mul_hi_i32 s56, s55, 0x2aaaaaab
	s_lshr_b32 s57, s56, 31
	s_ashr_i32 s56, s56, 3
	s_mul_hi_i32 s60, s55, 0x38e38e39
	s_add_i32 s56, s56, s57
	s_lshr_b32 s61, s60, 31
	s_ashr_i32 s60, s60, 7
	s_mul_i32 s57, s56, 0xffffffd0
	s_add_i32 s64, s60, s61
	s_add_i32 s57, s55, s57
	s_mul_i32 s60, s64, -12
	s_ashr_i32 s58, s57, 4
	s_and_b32 s59, s55, 15
	s_add_i32 s56, s60, s56
	s_cmp_lt_u32 s57, 16
	s_cselect_b64 s[60:61], -1, 0
	s_cmp_eq_u32 s58, 1
	s_cselect_b64 s[62:63], -1, 0
	s_bfe_u32 s57, s55, 0x20002
	s_and_b64 s[66:67], s[62:63], exec
	s_cselect_b32 s57, s57, s59
	s_and_b64 s[66:67], s[60:61], exec
	s_cselect_b32 s57, 0, s57
	s_and_b32 s65, s55, 3
	s_and_b64 s[66:67], s[62:63], exec
	s_cselect_b32 s65, s65, 0
	s_and_b64 s[66:67], s[60:61], exec
	s_cselect_b32 s59, s59, s65
	s_ashr_i32 s65, s64, 31
	s_lshl_b64 s[64:65], s[64:65], 11
	s_or_b32 s66, s64, s57
	s_lshl_b32 s80, s59, 7
	s_mul_i32 s67, s66, 0x2800
	s_mul_hi_u32 s66, s66, 0x2800
	s_mul_i32 s68, s65, 0x2800
	s_add_i32 s82, s80, 0xffffff80
	s_add_i32 s66, s66, s68
	s_add_u32 s68, s3, s67
	s_addc_u32 s69, s33, s66
	s_lshl_b32 s66, s56, 7
	s_ashr_i32 s67, s66, 31
	s_lshl_b64 s[66:67], s[66:67], 1
	s_add_u32 s68, s68, s66
	s_addc_u32 s69, s69, s67
	s_and_b64 s[70:71], s[62:63], exec
	s_movk_i32 s70, 0x5000
	s_cselect_b32 s81, s70, 0x14000
	s_and_b64 s[70:71], s[60:61], exec
	s_cselect_b32 s83, 0x1400, s81
	v_add_u32_e32 v50, s80, v58
	v_mad_u64_u32 v[120:121], s[70:71], s83, v50, 0
	s_and_b64 s[70:71], s[62:63], exec
	s_movk_i32 s70, 0x7f
	s_cselect_b32 s80, 0x1ff, s70
	s_and_b64 s[70:71], s[60:61], exec
	s_cselect_b32 s84, 0x7ff, s80
	v_or_b32_e32 v2, s82, v59
	s_cmp_eq_u32 s59, 0
	v_or_b32_e32 v10, s82, v60
	s_cselect_b64 s[70:71], -1, 0
	v_min_i32_e32 v2, s84, v2
	v_min_i32_e32 v10, s84, v10
	v_mov_b32_e32 v53, v51
	v_cndmask_b32_e64 v2, v2, 0, s[70:71]
	v_cndmask_b32_e64 v10, v10, 0, s[70:71]
	v_lshl_add_u64 v[112:113], s[68:69], 0, v[140:141]
	v_mad_u64_u32 v[2:3], s[80:81], s83, v2, 0
	v_mad_u64_u32 v[10:11], s[80:81], s83, v10, 0
	v_lshl_add_u64 v[6:7], v[2:3], 1, v[112:113]
	v_lshl_add_u64 v[14:15], v[10:11], 1, v[112:113]
	v_or_b32_e32 v18, s82, v61
	s_mov_b32 m0, s86
	s_nop 0
	global_load_lds_dwordx4 v[6:7], off
	s_add_i32 m0, s86, 8192
	s_nop 0
	global_load_lds_dwordx4 v[14:15], off
	v_add_co_u32_e32 v6, vcc, v144, v6
	v_min_i32_e32 v18, s84, v18
	v_add_u32_e32 v34, s82, v63
	v_addc_co_u32_e32 v7, vcc, 0, v7, vcc
	v_cndmask_b32_e64 v18, v18, 0, s[70:71]
	v_min_i32_e32 v34, s84, v34
	v_add_co_u32_e32 v14, vcc, v144, v14
	v_mad_u64_u32 v[18:19], s[70:71], s83, v18, 0
	v_mad_u64_u32 v[34:35], s[70:71], s83, v34, 0
	v_addc_co_u32_e32 v15, vcc, 0, v15, vcc
	v_lshl_add_u64 v[22:23], v[18:19], 1, v[112:113]
	v_lshl_add_u64 v[38:39], v[34:35], 1, v[112:113]
	s_add_i32 m0, s86, 16384
	s_nop 0
	global_load_lds_dwordx4 v[22:23], off
	s_add_i32 m0, s86, 32768
	s_nop 0
	global_load_lds_dwordx4 v[38:39], off
	v_add_co_u32_e32 v22, vcc, v144, v22
	v_or_b32_e32 v26, s82, v62
	s_nop 0
	v_addc_co_u32_e32 v23, vcc, 0, v23, vcc
	s_mov_b32 m0, s87
	s_nop 0
	global_load_lds_dwordx4 v[6:7], off
	v_min_i32_e32 v27, s84, v26
	v_cmp_lt_i32_e32 vcc, -1, v26
	v_add_u32_e32 v42, s82, v64
	v_min_i32_e32 v42, s84, v42
	v_cndmask_b32_e32 v26, 0, v27, vcc
	s_add_i32 m0, s87, 8192
	s_nop 0
	global_load_lds_dwordx4 v[14:15], off
	v_mad_u64_u32 v[26:27], s[70:71], s83, v26, 0
	v_mad_u64_u32 v[42:43], s[70:71], s83, v42, 0
	v_lshl_add_u64 v[30:31], v[26:27], 1, v[112:113]
	v_lshl_add_u64 v[46:47], v[42:43], 1, v[112:113]
	s_add_i32 m0, s87, 16384
	s_nop 0
	global_load_lds_dwordx4 v[22:23], off
	v_add_u32_e32 v53, s82, v65
	s_add_i32 m0, s86, 24576
	s_nop 0
	global_load_lds_dwordx4 v[30:31], off
	s_add_i32 m0, s86, 40960
	s_nop 0
	global_load_lds_dwordx4 v[46:47], off
	v_add_co_u32_e32 v30, vcc, v144, v30
	v_min_i32_e32 v53, s84, v53
	s_nop 0
	v_addc_co_u32_e32 v31, vcc, 0, v31, vcc
	s_add_i32 m0, s87, 24576
	s_nop 0
	global_load_lds_dwordx4 v[30:31], off
	v_add_co_u32_e32 v38, vcc, v144, v38
	v_mad_u64_u32 v[104:105], s[70:71], s83, v53, 0
	v_add_u32_e32 v53, s82, v66
	v_addc_co_u32_e32 v39, vcc, 0, v39, vcc
	v_min_i32_e32 v53, s84, v53
	s_add_i32 m0, s87, 32768
	s_nop 0
	global_load_lds_dwordx4 v[38:39], off
	v_add_co_u32_e32 v46, vcc, v144, v46
	v_mad_u64_u32 v[114:115], s[70:71], s83, v53, 0
	s_nop 0
	v_addc_co_u32_e32 v47, vcc, 0, v47, vcc
	v_lshl_add_u64 v[108:109], v[104:105], 1, v[112:113]
	v_lshl_add_u64 v[116:117], v[114:115], 1, v[112:113]
	s_add_i32 m0, s87, 40960
	s_nop 0
	global_load_lds_dwordx4 v[46:47], off
	v_mov_b32_e32 v55, v51
	s_add_i32 m0, s86, 49152
	s_nop 0
	global_load_lds_dwordx4 v[108:109], off
	s_add_i32 m0, s86, 57344
	s_nop 0
	global_load_lds_dwordx4 v[116:117], off
	v_add_co_u32_e32 v108, vcc, v144, v108
	s_nop 0
	v_addc_co_u32_e32 v109, vcc, 0, v109, vcc
	s_add_i32 m0, s87, 49152
	s_nop 0
	global_load_lds_dwordx4 v[108:109], off
	v_add_co_u32_e32 v116, vcc, v144, v116
	s_nop 0
	v_addc_co_u32_e32 v117, vcc, 0, v117, vcc
	s_add_i32 m0, s87, 57344
	s_nop 0
	global_load_lds_dwordx4 v[116:117], off
	v_lshl_add_u64 v[2:3], v[120:121], 1, s[68:69]
	v_lshl_add_u64 v[2:3], v[2:3], 0, v[54:55]
	global_load_dwordx4 v[46:49], v[2:3], off
	global_load_dwordx4 v[42:45], v[2:3], off offset:64
	global_load_dwordx4 v[38:41], v[2:3], off offset:128
	global_load_dwordx4 v[6:9], v[2:3], off offset:192
	s_waitcnt vmcnt(4)
	s_waitcnt lgkmcnt(0)
	s_barrier
	s_cmp_lg_u32 s59, 0
	s_mov_b32 s59, 0xff800000
	s_cselect_b64 s[68:69], -1, 0
	s_or_b64 s[70:71], s[68:69], s[26:27]
	s_and_b64 vcc, s[70:71], s[6:7]
	ds_read_b128 v[132:135], v96
	ds_read_b128 v[136:139], v97
	ds_read_b128 v[152:155], v98
	ds_read_b128 v[168:171], v99
	ds_read_b128 v[172:175], v96 offset:4096
	ds_read_b128 v[176:179], v97 offset:4096
	ds_read_b128 v[180:183], v98 offset:4096
	ds_read_b128 v[192:195], v99 offset:4096
	ds_read_b128 v[196:199], v96 offset:8192
	ds_read_b128 v[200:203], v97 offset:8192
	ds_read_b128 v[204:207], v98 offset:8192
	ds_read_b128 v[208:211], v99 offset:8192
	ds_read_b128 v[212:215], v96 offset:12288
	ds_read_b128 v[216:219], v97 offset:12288
	ds_read_b128 v[220:223], v98 offset:12288
	s_waitcnt vmcnt(3) lgkmcnt(14)
	v_mfma_f32_16x16x32_bf16 v[2:5], v[132:135], v[46:49], 0
	ds_read_b128 v[228:231], v99 offset:12288
	s_waitcnt vmcnt(2) lgkmcnt(14)
	v_mfma_f32_16x16x32_bf16 v[2:5], v[136:139], v[42:45], v[2:5]
	ds_read_b128 v[132:135], v96 offset:16384
	s_waitcnt vmcnt(1) lgkmcnt(14)
	v_mfma_f32_16x16x32_bf16 v[2:5], v[152:155], v[38:41], v[2:5]
	ds_read_b128 v[136:139], v97 offset:16384
	s_waitcnt vmcnt(0) lgkmcnt(14)
	v_mfma_f32_16x16x32_bf16 v[2:5], v[168:171], v[6:9], v[2:5]
	ds_read_b128 v[152:155], v98 offset:16384
	s_waitcnt lgkmcnt(14)
	v_mfma_f32_16x16x32_bf16 v[10:13], v[172:175], v[46:49], 0
	ds_read_b128 v[168:171], v99 offset:16384
	s_waitcnt lgkmcnt(14)
	v_mfma_f32_16x16x32_bf16 v[10:13], v[176:179], v[42:45], v[10:13]
	ds_read_b128 v[172:175], v96 offset:20480
	s_waitcnt lgkmcnt(14)
	v_mfma_f32_16x16x32_bf16 v[10:13], v[180:183], v[38:41], v[10:13]
	ds_read_b128 v[176:179], v97 offset:20480
	s_waitcnt lgkmcnt(14)
	v_mfma_f32_16x16x32_bf16 v[10:13], v[192:195], v[6:9], v[10:13]
	ds_read_b128 v[180:183], v98 offset:20480
	s_waitcnt lgkmcnt(14)
	v_mfma_f32_16x16x32_bf16 v[14:17], v[196:199], v[46:49], 0
	ds_read_b128 v[192:195], v99 offset:20480
	s_waitcnt lgkmcnt(14)
	v_mfma_f32_16x16x32_bf16 v[14:17], v[200:203], v[42:45], v[14:17]
	ds_read_b128 v[196:199], v96 offset:24576
	s_waitcnt lgkmcnt(14)
	v_mfma_f32_16x16x32_bf16 v[14:17], v[204:207], v[38:41], v[14:17]
	ds_read_b128 v[200:203], v97 offset:24576
	s_waitcnt lgkmcnt(14)
	v_mfma_f32_16x16x32_bf16 v[14:17], v[208:211], v[6:9], v[14:17]
	ds_read_b128 v[204:207], v98 offset:24576
	s_waitcnt lgkmcnt(14)
	v_mfma_f32_16x16x32_bf16 v[18:21], v[212:215], v[46:49], 0
	ds_read_b128 v[208:211], v99 offset:24576
	s_waitcnt lgkmcnt(14)
	v_mfma_f32_16x16x32_bf16 v[18:21], v[216:219], v[42:45], v[18:21]
	ds_read_b128 v[212:215], v96 offset:28672
	s_waitcnt lgkmcnt(14)
	v_mfma_f32_16x16x32_bf16 v[18:21], v[220:223], v[38:41], v[18:21]
	ds_read_b128 v[216:219], v97 offset:28672
	s_waitcnt lgkmcnt(14)
	v_mfma_f32_16x16x32_bf16 v[18:21], v[228:231], v[6:9], v[18:21]
	ds_read_b128 v[220:223], v98 offset:28672
	s_waitcnt lgkmcnt(14)
	v_mfma_f32_16x16x32_bf16 v[22:25], v[132:135], v[46:49], 0
	ds_read_b128 v[228:231], v99 offset:28672
	s_waitcnt lgkmcnt(14)
	v_mfma_f32_16x16x32_bf16 v[22:25], v[136:139], v[42:45], v[22:25]
	ds_read_b128 v[132:135], v96 offset:32768
	s_waitcnt lgkmcnt(14)
	v_mfma_f32_16x16x32_bf16 v[22:25], v[152:155], v[38:41], v[22:25]
	ds_read_b128 v[136:139], v97 offset:32768
	s_waitcnt lgkmcnt(14)
	v_mfma_f32_16x16x32_bf16 v[22:25], v[168:171], v[6:9], v[22:25]
	ds_read_b128 v[152:155], v98 offset:32768
	s_waitcnt lgkmcnt(14)
	v_mfma_f32_16x16x32_bf16 v[26:29], v[172:175], v[46:49], 0
	ds_read_b128 v[168:171], v99 offset:32768
	s_waitcnt lgkmcnt(14)
	v_mfma_f32_16x16x32_bf16 v[26:29], v[176:179], v[42:45], v[26:29]
	s_waitcnt lgkmcnt(13)
	v_mfma_f32_16x16x32_bf16 v[26:29], v[180:183], v[38:41], v[26:29]
	s_waitcnt lgkmcnt(12)
	v_mfma_f32_16x16x32_bf16 v[26:29], v[192:195], v[6:9], v[26:29]
	s_waitcnt lgkmcnt(11)
	v_mfma_f32_16x16x32_bf16 v[30:33], v[196:199], v[46:49], 0
	s_waitcnt lgkmcnt(10)
	v_mfma_f32_16x16x32_bf16 v[30:33], v[200:203], v[42:45], v[30:33]
	s_waitcnt lgkmcnt(9)
	v_mfma_f32_16x16x32_bf16 v[30:33], v[204:207], v[38:41], v[30:33]
	s_waitcnt lgkmcnt(8)
	v_mfma_f32_16x16x32_bf16 v[30:33], v[208:211], v[6:9], v[30:33]
	s_waitcnt lgkmcnt(7)
	v_mfma_f32_16x16x32_bf16 v[34:37], v[212:215], v[46:49], 0
	s_waitcnt lgkmcnt(6)
	v_mfma_f32_16x16x32_bf16 v[34:37], v[216:219], v[42:45], v[34:37]
	s_waitcnt lgkmcnt(5)
	v_mfma_f32_16x16x32_bf16 v[34:37], v[220:223], v[38:41], v[34:37]
	s_waitcnt lgkmcnt(4)
	v_mfma_f32_16x16x32_bf16 v[34:37], v[228:231], v[6:9], v[34:37]
	s_waitcnt lgkmcnt(3)
	v_mfma_f32_16x16x32_bf16 v[104:107], v[132:135], v[46:49], 0
	s_waitcnt lgkmcnt(2)
	v_mfma_f32_16x16x32_bf16 v[104:107], v[136:139], v[42:45], v[104:107]
	s_waitcnt lgkmcnt(1)
	v_mfma_f32_16x16x32_bf16 v[104:107], v[152:155], v[38:41], v[104:107]
	s_waitcnt lgkmcnt(0)
	v_mfma_f32_16x16x32_bf16 v[6:9], v[168:171], v[6:9], v[104:107]
	s_nop 2
	v_cndmask_b32_e32 v38, v101, v2, vcc
	s_and_b64 vcc, s[70:71], s[8:9]
	v_cndmask_b32_e32 v39, v101, v3, vcc
	s_and_b64 vcc, s[70:71], s[10:11]
	v_cndmask_b32_e32 v4, v101, v4, vcc
	s_and_b64 vcc, s[70:71], s[12:13]
	v_max3_f32 v2, v38, s59, v39
	v_cndmask_b32_e32 v5, v101, v5, vcc
	s_or_b64 vcc, s[28:29], s[68:69]
	v_max3_f32 v2, v2, v4, v5
	v_cndmask_b32_e32 v10, v101, v10, vcc
	v_cndmask_b32_e32 v11, v101, v11, vcc
	v_max3_f32 v2, v2, v10, v11
	v_cndmask_b32_e32 v12, v101, v12, vcc
	v_cndmask_b32_e32 v13, v101, v13, vcc
	s_or_b64 vcc, s[30:31], s[68:69]
	v_max3_f32 v2, v2, v12, v13
	v_cndmask_b32_e32 v14, v101, v14, vcc
	v_cndmask_b32_e32 v15, v101, v15, vcc
	v_max3_f32 v2, v2, v14, v15
	v_cndmask_b32_e32 v16, v101, v16, vcc
	v_cndmask_b32_e32 v17, v101, v17, vcc
	s_or_b64 vcc, s[34:35], s[68:69]
	v_max3_f32 v2, v2, v16, v17
	v_cndmask_b32_e32 v40, v101, v18, vcc
	v_cndmask_b32_e32 v41, v101, v19, vcc
	v_max3_f32 v2, v2, v40, v41
	v_cndmask_b32_e32 v20, v101, v20, vcc
	v_cndmask_b32_e32 v21, v101, v21, vcc
	s_or_b64 vcc, s[36:37], s[68:69]
	v_max3_f32 v2, v2, v20, v21
	v_cndmask_b32_e32 v22, v101, v22, vcc
	v_cndmask_b32_e32 v23, v101, v23, vcc
	v_max3_f32 v2, v2, v22, v23
	v_cndmask_b32_e32 v24, v101, v24, vcc
	v_cndmask_b32_e32 v42, v101, v25, vcc
	s_or_b64 vcc, s[38:39], s[68:69]
	v_max3_f32 v2, v2, v24, v42
	v_cndmask_b32_e32 v43, v101, v26, vcc
	v_cndmask_b32_e32 v44, v101, v27, vcc
	v_max3_f32 v2, v2, v43, v44
	v_cndmask_b32_e32 v45, v101, v28, vcc
	v_cndmask_b32_e32 v46, v101, v29, vcc
	s_or_b64 vcc, s[40:41], s[68:69]
	v_max3_f32 v2, v2, v45, v46
	v_cndmask_b32_e32 v47, v101, v30, vcc
	v_cndmask_b32_e32 v48, v101, v31, vcc
	v_max3_f32 v2, v2, v47, v48
	v_cndmask_b32_e32 v49, v101, v32, vcc
	v_cndmask_b32_e32 v53, v101, v33, vcc
	s_or_b64 vcc, s[42:43], s[68:69]
	v_max3_f32 v2, v2, v49, v53
	v_cndmask_b32_e32 v55, v101, v34, vcc
	v_cndmask_b32_e32 v57, v101, v35, vcc
	v_max3_f32 v2, v2, v55, v57
	v_cndmask_b32_e32 v103, v101, v36, vcc
	v_cndmask_b32_e32 v104, v101, v37, vcc
	v_max3_f32 v2, v2, v103, v104
	v_cndmask_b32_e64 v6, v101, v6, s[14:15]
	v_cndmask_b32_e64 v7, v101, v7, s[16:17]
	v_and_b32_e32 v18, 64, v100
	v_max3_f32 v3, v2, v6, v7
	v_cndmask_b32_e64 v2, v101, v9, s[20:21]
	v_xor_b32_e32 v9, 16, v100
	v_add_u32_e32 v18, 64, v18
	v_cmp_lt_i32_e32 vcc, v9, v18
	v_cndmask_b32_e64 v8, v101, v8, s[18:19]
	v_max3_f32 v3, v3, v8, v2
	v_cndmask_b32_e32 v9, v100, v9, vcc
	v_lshlrev_b32_e32 v105, 2, v9
	ds_bpermute_b32 v9, v105, v3
	s_and_b64 s[62:63], s[62:63], exec
	s_cselect_b32 s59, 2, 4
	s_and_b64 s[60:61], s[60:61], exec
	s_cselect_b32 s59, 0, s59
	s_waitcnt lgkmcnt(0)
	v_max_f32_e32 v9, v9, v9
	v_max_f32_e32 v3, v3, v9
	v_xor_b32_e32 v9, 32, v100
	v_cmp_lt_i32_e32 vcc, v9, v18
	s_nop 1
	v_cndmask_b32_e32 v9, v100, v9, vcc
	v_lshlrev_b32_e32 v106, 2, v9
	ds_bpermute_b32 v9, v106, v3
	s_waitcnt lgkmcnt(0)
	v_max_f32_e32 v9, v9, v9
	v_max_f32_e32 v3, v3, v9
	v_pk_mul_f32 v[18:19], v[2:3], s[54:55] op_sel_hi:[1,0]
	s_nop 0
	v_fma_f32 v4, v4, s54, -v19
	v_exp_f32_e32 v109, v4
	v_fma_f32 v4, v5, s54, -v19
	v_exp_f32_e32 v110, v4
	v_fma_f32 v4, v10, s54, -v19
	v_exp_f32_e32 v111, v4
	v_fma_f32 v4, v11, s54, -v19
	v_exp_f32_e32 v112, v4
	v_fma_f32 v4, v12, s54, -v19
	v_fma_f32 v2, v38, s54, -v19
	v_exp_f32_e32 v113, v4
	v_fma_f32 v4, v13, s54, -v19
	v_exp_f32_e32 v107, v2
	v_fma_f32 v9, v39, s54, -v19
	v_exp_f32_e32 v114, v4
	v_fma_f32 v4, v14, s54, -v19
	v_exp_f32_e32 v108, v9
	v_exp_f32_e32 v33, v4
	v_fma_f32 v4, v15, s54, -v19
	v_exp_f32_e32 v34, v4
	v_fma_f32 v4, v16, s54, -v19
	v_exp_f32_e32 v35, v4
	v_fma_f32 v4, v17, s54, -v19
	v_add_f32_e32 v2, 0, v107
	v_exp_f32_e32 v36, v4
	v_fma_f32 v4, v40, s54, -v19
	v_add_f32_e32 v2, v108, v2
	v_exp_f32_e32 v37, v4
	v_fma_f32 v4, v41, s54, -v19
	v_add_f32_e32 v2, v109, v2
	v_exp_f32_e32 v38, v4
	v_fma_f32 v4, v20, s54, -v19
	v_add_f32_e32 v2, v110, v2
	v_exp_f32_e32 v39, v4
	v_fma_f32 v4, v21, s54, -v19
	v_add_f32_e32 v2, v111, v2
	v_exp_f32_e32 v40, v4
	v_fma_f32 v4, v22, s54, -v19
	v_add_f32_e32 v2, v112, v2
	v_exp_f32_e32 v25, v4
	v_fma_f32 v4, v23, s54, -v19
	v_add_f32_e32 v2, v113, v2
	v_exp_f32_e32 v26, v4
	v_fma_f32 v4, v24, s54, -v19
	v_add_f32_e32 v2, v114, v2
	v_exp_f32_e32 v27, v4
	v_fma_f32 v4, v42, s54, -v19
	v_add_f32_e32 v2, v33, v2
	v_exp_f32_e32 v28, v4
	v_fma_f32 v4, v43, s54, -v19
	v_add_f32_e32 v2, v34, v2
	v_exp_f32_e32 v29, v4
	v_fma_f32 v4, v44, s54, -v19
	v_add_f32_e32 v2, v35, v2
	v_exp_f32_e32 v30, v4
	v_fma_f32 v4, v45, s54, -v19
	v_add_f32_e32 v2, v36, v2
	v_exp_f32_e32 v31, v4
	v_fma_f32 v4, v46, s54, -v19
	v_add_f32_e32 v2, v37, v2
	v_exp_f32_e32 v32, v4
	v_fma_f32 v4, v47, s54, -v19
	v_add_f32_e32 v2, v38, v2
	v_exp_f32_e32 v9, v4
	v_fma_f32 v4, v48, s54, -v19
	v_add_f32_e32 v2, v39, v2
	v_exp_f32_e32 v10, v4
	v_fma_f32 v4, v49, s54, -v19
	v_add_f32_e32 v2, v40, v2
	v_exp_f32_e32 v11, v4
	v_fma_f32 v4, v53, s54, -v19
	v_add_f32_e32 v2, v25, v2
	v_exp_f32_e32 v12, v4
	v_fma_f32 v4, v55, s54, -v19
	v_add_f32_e32 v2, v26, v2
	v_exp_f32_e32 v13, v4
	v_fma_f32 v4, v57, s54, -v19
	v_add_f32_e32 v2, v27, v2
	v_exp_f32_e32 v14, v4
	v_fma_f32 v4, v103, s54, -v19
	v_add_f32_e32 v2, v28, v2
	v_exp_f32_e32 v15, v4
	v_fma_f32 v4, v104, s54, -v19
	v_add_f32_e32 v2, v29, v2
	v_exp_f32_e32 v16, v4
	v_fma_f32 v4, v6, s54, -v19
	v_add_f32_e32 v2, v30, v2
	v_exp_f32_e32 v5, v4
	v_fma_f32 v4, v7, s54, -v19
	v_add_f32_e32 v2, v31, v2
	v_exp_f32_e32 v6, v4
	v_fma_f32 v4, v8, s54, -v19
	v_add_f32_e32 v2, v32, v2
	v_exp_f32_e32 v7, v4
	v_sub_f32_e32 v4, v18, v19
	v_add_u32_e32 v124, v67, v69
	v_add_u32_e32 v125, v67, v70
	v_add_u32_e32 v126, v67, v71
	v_add_u32_e32 v127, v67, v72
	v_add_u32_e32 v128, v67, v73
	v_add_u32_e32 v129, v67, v74
	v_add_u32_e32 v130, v67, v75
	v_add_u32_e32 v131, v67, v76
	ds_read_b64_tr_b16 v[196:197], v124
	ds_read_b64_tr_b16 v[198:199], v124 offset:4096
	ds_read_b64_tr_b16 v[200:201], v125
	ds_read_b64_tr_b16 v[202:203], v125 offset:4096
	ds_read_b64_tr_b16 v[204:205], v126
	ds_read_b64_tr_b16 v[206:207], v126 offset:4096
	ds_read_b64_tr_b16 v[208:209], v127
	ds_read_b64_tr_b16 v[210:211], v127 offset:4096
	ds_read_b64_tr_b16 v[212:213], v128
	ds_read_b64_tr_b16 v[214:215], v128 offset:4096
	ds_read_b64_tr_b16 v[216:217], v129
	ds_read_b64_tr_b16 v[218:219], v129 offset:4096
	ds_read_b64_tr_b16 v[220:221], v130
	ds_read_b64_tr_b16 v[222:223], v130 offset:4096
	v_cvt_pk_bf16_f32 v42, v107, v108
	v_cvt_pk_bf16_f32 v43, v109, v110
	v_cvt_pk_bf16_f32 v44, v111, v112
	v_cvt_pk_bf16_f32 v45, v113, v114
	v_add_f32_e32 v2, v9, v2
	v_add_f32_e32 v2, v10, v2
	v_add_f32_e32 v2, v11, v2
	v_add_f32_e32 v2, v12, v2
	v_add_f32_e32 v2, v13, v2
	v_add_f32_e32 v2, v14, v2
	v_add_f32_e32 v2, v15, v2
	v_add_f32_e32 v2, v16, v2
	v_exp_f32_e32 v8, v4
	v_add_f32_e32 v2, v5, v2
	v_add_f32_e32 v2, v6, v2
	v_add_f32_e32 v2, v7, v2
	v_cvt_pk_bf16_f32 v34, v33, v34
	v_cvt_pk_bf16_f32 v35, v35, v36
	v_cvt_pk_bf16_f32 v36, v37, v38
	v_cvt_pk_bf16_f32 v37, v39, v40
	v_add_f32_e32 v2, v8, v2
	ds_bpermute_b32 v4, v105, v2
	v_cvt_pk_bf16_f32 v26, v25, v26
	v_cvt_pk_bf16_f32 v27, v27, v28
	v_cvt_pk_bf16_f32 v28, v29, v30
	v_cvt_pk_bf16_f32 v29, v31, v32
	v_cvt_pk_bf16_f32 v10, v9, v10
	v_cvt_pk_bf16_f32 v11, v11, v12
	v_cvt_pk_bf16_f32 v12, v13, v14
	v_cvt_pk_bf16_f32 v13, v15, v16
	s_waitcnt lgkmcnt(0)
	v_add_f32_e32 v2, v2, v4
	ds_bpermute_b32 v4, v106, v2
	v_cvt_pk_bf16_f32 v6, v5, v6
	v_cvt_pk_bf16_f32 v7, v7, v8
	v_mov_b32_e32 v8, v51
	v_mov_b32_e32 v9, v51
	v_mov_b32_e32 v57, v51
	s_waitcnt lgkmcnt(0)
	v_add_f32_e32 v2, v2, v4
	v_div_scale_f32 v4, s[68:69], v2, v2, 1.0
	v_rcp_f32_e32 v5, v4
	v_mfma_f32_16x16x32_bf16 v[132:135], v[196:199], v[42:45], 0
	ds_read_b64_tr_b16 v[228:229], v131
	ds_read_b64_tr_b16 v[230:231], v131 offset:4096
	v_mfma_f32_16x16x32_bf16 v[136:139], v[200:203], v[42:45], 0
	ds_read_b64_tr_b16 v[196:197], v124 offset:8192
	ds_read_b64_tr_b16 v[198:199], v124 offset:12288
	v_mfma_f32_16x16x32_bf16 v[152:155], v[204:207], v[42:45], 0
	ds_read_b64_tr_b16 v[200:201], v125 offset:8192
	ds_read_b64_tr_b16 v[202:203], v125 offset:12288
	v_mfma_f32_16x16x32_bf16 v[168:171], v[208:211], v[42:45], 0
	ds_read_b64_tr_b16 v[204:205], v126 offset:8192
	ds_read_b64_tr_b16 v[206:207], v126 offset:12288
	v_mfma_f32_16x16x32_bf16 v[172:175], v[212:215], v[42:45], 0
	ds_read_b64_tr_b16 v[208:209], v127 offset:8192
	ds_read_b64_tr_b16 v[210:211], v127 offset:12288
	v_mfma_f32_16x16x32_bf16 v[176:179], v[216:219], v[42:45], 0
	ds_read_b64_tr_b16 v[212:213], v128 offset:8192
	ds_read_b64_tr_b16 v[214:215], v128 offset:12288
	v_mfma_f32_16x16x32_bf16 v[180:183], v[220:223], v[42:45], 0
	ds_read_b64_tr_b16 v[216:217], v129 offset:8192
	ds_read_b64_tr_b16 v[218:219], v129 offset:12288
	s_waitcnt lgkmcnt(12)
	v_mfma_f32_16x16x32_bf16 v[192:195], v[228:231], v[42:45], 0
	ds_read_b64_tr_b16 v[220:221], v130 offset:8192
	ds_read_b64_tr_b16 v[222:223], v130 offset:12288
	s_waitcnt lgkmcnt(12)
	v_mfma_f32_16x16x32_bf16 v[132:135], v[196:199], v[34:37], v[132:135]
	ds_read_b64_tr_b16 v[228:229], v131 offset:8192
	ds_read_b64_tr_b16 v[230:231], v131 offset:12288
	s_waitcnt lgkmcnt(12)
	v_mfma_f32_16x16x32_bf16 v[136:139], v[200:203], v[34:37], v[136:139]
	ds_read_b64_tr_b16 v[196:197], v124 offset:16384
	ds_read_b64_tr_b16 v[198:199], v124 offset:20480
	s_waitcnt lgkmcnt(12)
	v_mfma_f32_16x16x32_bf16 v[152:155], v[204:207], v[34:37], v[152:155]
	ds_read_b64_tr_b16 v[200:201], v125 offset:16384
	ds_read_b64_tr_b16 v[202:203], v125 offset:20480
	s_waitcnt lgkmcnt(12)
	v_mfma_f32_16x16x32_bf16 v[168:171], v[208:211], v[34:37], v[168:171]
	ds_read_b64_tr_b16 v[204:205], v126 offset:16384
	ds_read_b64_tr_b16 v[206:207], v126 offset:20480
	s_waitcnt lgkmcnt(12)
	v_mfma_f32_16x16x32_bf16 v[172:175], v[212:215], v[34:37], v[172:175]
	ds_read_b64_tr_b16 v[208:209], v127 offset:16384
	ds_read_b64_tr_b16 v[210:211], v127 offset:20480
	s_waitcnt lgkmcnt(12)
	v_mfma_f32_16x16x32_bf16 v[176:179], v[216:219], v[34:37], v[176:179]
	ds_read_b64_tr_b16 v[212:213], v128 offset:16384
	ds_read_b64_tr_b16 v[214:215], v128 offset:20480
	s_waitcnt lgkmcnt(12)
	v_mfma_f32_16x16x32_bf16 v[180:183], v[220:223], v[34:37], v[180:183]
	ds_read_b64_tr_b16 v[216:217], v129 offset:16384
	ds_read_b64_tr_b16 v[218:219], v129 offset:20480
	s_waitcnt lgkmcnt(12)
	v_mfma_f32_16x16x32_bf16 v[192:195], v[228:231], v[34:37], v[192:195]
	ds_read_b64_tr_b16 v[220:221], v130 offset:16384
	ds_read_b64_tr_b16 v[222:223], v130 offset:20480
	s_waitcnt lgkmcnt(12)
	v_mfma_f32_16x16x32_bf16 v[132:135], v[196:199], v[26:29], v[132:135]
	ds_read_b64_tr_b16 v[228:229], v131 offset:16384
	ds_read_b64_tr_b16 v[230:231], v131 offset:20480
	s_waitcnt lgkmcnt(12)
	v_mfma_f32_16x16x32_bf16 v[136:139], v[200:203], v[26:29], v[136:139]
	ds_read_b64_tr_b16 v[196:197], v124 offset:24576
	ds_read_b64_tr_b16 v[198:199], v124 offset:28672
	s_waitcnt lgkmcnt(12)
	v_mfma_f32_16x16x32_bf16 v[152:155], v[204:207], v[26:29], v[152:155]
	ds_read_b64_tr_b16 v[200:201], v125 offset:24576
	ds_read_b64_tr_b16 v[202:203], v125 offset:28672
	s_waitcnt lgkmcnt(12)
	v_mfma_f32_16x16x32_bf16 v[168:171], v[208:211], v[26:29], v[168:171]
	ds_read_b64_tr_b16 v[204:205], v126 offset:24576
	ds_read_b64_tr_b16 v[206:207], v126 offset:28672
	s_waitcnt lgkmcnt(12)
	v_mfma_f32_16x16x32_bf16 v[172:175], v[212:215], v[26:29], v[172:175]
	ds_read_b64_tr_b16 v[208:209], v127 offset:24576
	ds_read_b64_tr_b16 v[210:211], v127 offset:28672
	s_waitcnt lgkmcnt(12)
	v_mfma_f32_16x16x32_bf16 v[176:179], v[216:219], v[26:29], v[176:179]
	ds_read_b64_tr_b16 v[212:213], v128 offset:24576
	ds_read_b64_tr_b16 v[214:215], v128 offset:28672
	s_waitcnt lgkmcnt(12)
	v_mfma_f32_16x16x32_bf16 v[180:183], v[220:223], v[26:29], v[180:183]
	ds_read_b64_tr_b16 v[216:217], v129 offset:24576
	ds_read_b64_tr_b16 v[218:219], v129 offset:28672
	s_waitcnt lgkmcnt(12)
	v_mfma_f32_16x16x32_bf16 v[192:195], v[228:231], v[26:29], v[192:195]
	ds_read_b64_tr_b16 v[220:221], v130 offset:24576
	ds_read_b64_tr_b16 v[222:223], v130 offset:28672
	s_waitcnt lgkmcnt(12)
	v_mfma_f32_16x16x32_bf16 v[132:135], v[196:199], v[10:13], v[132:135]
	ds_read_b64_tr_b16 v[228:229], v131 offset:24576
	ds_read_b64_tr_b16 v[230:231], v131 offset:28672
	s_waitcnt lgkmcnt(12)
	v_mfma_f32_16x16x32_bf16 v[136:139], v[200:203], v[10:13], v[136:139]
	ds_read_b64_tr_b16 v[196:197], v124 offset:32768
	v_mov_b32_e32 v198, v51
	v_mov_b32_e32 v199, v51
	s_waitcnt lgkmcnt(11)
	v_mfma_f32_16x16x32_bf16 v[152:155], v[204:207], v[10:13], v[152:155]
	ds_read_b64_tr_b16 v[200:201], v125 offset:32768
	v_mov_b32_e32 v202, v51
	v_mov_b32_e32 v203, v51
	s_waitcnt lgkmcnt(10)
	v_mfma_f32_16x16x32_bf16 v[168:171], v[208:211], v[10:13], v[168:171]
	ds_read_b64_tr_b16 v[204:205], v126 offset:32768
	v_mov_b32_e32 v206, v51
	v_mov_b32_e32 v207, v51
	s_waitcnt lgkmcnt(9)
	v_mfma_f32_16x16x32_bf16 v[172:175], v[212:215], v[10:13], v[172:175]
	ds_read_b64_tr_b16 v[208:209], v127 offset:32768
	v_mov_b32_e32 v210, v51
	v_mov_b32_e32 v211, v51
	s_waitcnt lgkmcnt(8)
	v_mfma_f32_16x16x32_bf16 v[176:179], v[216:219], v[10:13], v[176:179]
	ds_read_b64_tr_b16 v[212:213], v128 offset:32768
	v_mov_b32_e32 v214, v51
	v_mov_b32_e32 v215, v51
	s_waitcnt lgkmcnt(7)
	v_mfma_f32_16x16x32_bf16 v[180:183], v[220:223], v[10:13], v[180:183]
	ds_read_b64_tr_b16 v[216:217], v129 offset:32768
	v_mov_b32_e32 v218, v51
	v_mov_b32_e32 v219, v51
	s_waitcnt lgkmcnt(6)
	v_mfma_f32_16x16x32_bf16 v[192:195], v[228:231], v[10:13], v[192:195]
	ds_read_b64_tr_b16 v[220:221], v130 offset:32768
	v_mov_b32_e32 v222, v51
	v_mov_b32_e32 v223, v51
	s_waitcnt lgkmcnt(6)
	v_mfma_f32_16x16x32_bf16 v[14:17], v[196:199], v[6:9], v[132:135]
	ds_read_b64_tr_b16 v[228:229], v131 offset:32768
	v_mov_b32_e32 v230, v51
	v_mov_b32_e32 v231, v51
	s_waitcnt lgkmcnt(6)
	v_mfma_f32_16x16x32_bf16 v[26:29], v[200:203], v[6:9], v[136:139]
	s_waitcnt lgkmcnt(5)
	v_mfma_f32_16x16x32_bf16 v[30:33], v[204:207], v[6:9], v[152:155]
	s_waitcnt lgkmcnt(4)
	v_mfma_f32_16x16x32_bf16 v[34:37], v[208:211], v[6:9], v[168:171]
	s_waitcnt lgkmcnt(3)
	v_mfma_f32_16x16x32_bf16 v[18:21], v[212:215], v[6:9], v[172:175]
	s_waitcnt lgkmcnt(2)
	v_mfma_f32_16x16x32_bf16 v[38:41], v[216:219], v[6:9], v[176:179]
	s_waitcnt lgkmcnt(1)
	v_mfma_f32_16x16x32_bf16 v[42:45], v[220:223], v[6:9], v[180:183]
	s_waitcnt lgkmcnt(0)
	v_mfma_f32_16x16x32_bf16 v[6:9], v[228:231], v[6:9], v[192:195]
	s_nop 2
	v_fma_f32 v10, -v4, v5, 1.0
	v_fmac_f32_e32 v5, v10, v5
	v_div_scale_f32 v10, vcc, 1.0, v2, 1.0
	v_mul_f32_e32 v11, v10, v5
	v_fma_f32 v12, -v4, v11, v10
	v_fmac_f32_e32 v11, v12, v5
	v_fma_f32 v4, -v4, v11, v10
	v_div_fmas_f32 v4, v4, v5, v11
	v_div_fixup_f32 v22, v4, v2, 1.0
	v_lshlrev_b64 v[4:5], s59, v[50:51]
	s_ashr_i32 s59, s58, 31
	s_lshl_b64 s[58:59], s[58:59], 14
	s_add_u32 s58, s58, s64
	s_addc_u32 s59, s59, s65
	s_or_b32 s58, s58, s57
	v_lshl_add_u64 v[4:5], s[58:59], 0, v[4:5]
	v_mov_b64_e32 v[10:11], s[22:23]
	v_mad_u64_u32 v[10:11], s[58:59], v4, s45, v[10:11]
	v_mad_i32_i24 v11, v5, s45, v11
	v_mul_f32_e32 v12, v22, v14
	v_mul_f32_e32 v13, v22, v15
	v_lshl_add_u64 v[10:11], v[10:11], 0, s[66:67]
	v_cvt_pk_bf16_f32 v12, v12, v13
	v_mul_f32_e32 v13, v22, v16
	v_lshl_add_u64 v[10:11], v[10:11], 0, v[56:57]
	v_mul_f32_e32 v14, v22, v17
	v_cvt_pk_bf16_f32 v13, v13, v14
	global_store_dwordx2 v[10:11], v[12:13], off
	v_mul_f32_e32 v12, v22, v26
	v_mul_f32_e32 v13, v22, v27
	v_cvt_pk_bf16_f32 v12, v12, v13
	v_mul_f32_e32 v13, v22, v28
	v_mul_f32_e32 v14, v22, v29
	v_cvt_pk_bf16_f32 v13, v13, v14
	global_store_dwordx2 v[10:11], v[12:13], off offset:32
	v_mul_f32_e32 v12, v22, v30
	v_mul_f32_e32 v13, v22, v31
	v_cvt_pk_bf16_f32 v12, v12, v13
	v_mul_f32_e32 v13, v22, v32
	v_mul_f32_e32 v14, v22, v33
	v_cvt_pk_bf16_f32 v13, v13, v14
	global_store_dwordx2 v[10:11], v[12:13], off offset:64
	v_mul_f32_e32 v12, v22, v34
	v_mul_f32_e32 v13, v22, v35
	v_cvt_pk_bf16_f32 v12, v12, v13
	v_mul_f32_e32 v13, v22, v36
	v_mul_f32_e32 v14, v22, v37
	v_cvt_pk_bf16_f32 v13, v13, v14
	global_store_dwordx2 v[10:11], v[12:13], off offset:96
	v_mul_f32_e32 v12, v22, v18
	v_mul_f32_e32 v13, v22, v19
	v_cvt_pk_bf16_f32 v12, v12, v13
	v_mul_f32_e32 v13, v22, v20
	v_mul_f32_e32 v14, v22, v21
	v_cvt_pk_bf16_f32 v13, v13, v14
	global_store_dwordx2 v[10:11], v[12:13], off offset:128
	v_mul_f32_e32 v12, v22, v38
	v_mul_f32_e32 v13, v22, v39
	v_cvt_pk_bf16_f32 v12, v12, v13
	v_mul_f32_e32 v13, v22, v40
	v_mul_f32_e32 v14, v22, v41
	v_cvt_pk_bf16_f32 v13, v13, v14
	global_store_dwordx2 v[10:11], v[12:13], off offset:160
	v_mul_f32_e32 v12, v22, v42
	v_mul_f32_e32 v13, v22, v43
	v_cvt_pk_bf16_f32 v12, v12, v13
	v_mul_f32_e32 v13, v22, v44
	v_mul_f32_e32 v6, v22, v6
	v_mul_f32_e32 v7, v22, v7
	v_mul_f32_e32 v14, v22, v45
	v_cvt_pk_bf16_f32 v13, v13, v14
	global_store_dwordx2 v[10:11], v[12:13], off offset:192
	v_cvt_pk_bf16_f32 v6, v6, v7
	v_mul_f32_e32 v7, v22, v8
	v_mul_f32_e32 v8, v22, v9
	v_cvt_pk_bf16_f32 v7, v7, v8
	global_store_dwordx2 v[10:11], v[6:7], off offset:224
	s_and_saveexec_b64 s[58:59], s[4:5]
	s_cbranch_execz .LBB0_242
	s_mov_b32 s57, 0x800000
	v_cmp_gt_f32_e32 vcc, s57, v2
	s_mov_b32 s57, 0x3f317217
	s_nop 0
	v_cndmask_b32_e64 v6, 0, 32, vcc
	v_ldexp_f32 v2, v2, v6
	v_log_f32_e32 v2, v2
	v_cndmask_b32_e32 v6, 0, v102, vcc
	v_mul_f32_e32 v7, 0x3f317217, v2
	v_fma_f32 v7, v2, s57, -v7
	v_fmac_f32_e32 v7, 0x3377d1cf, v2
	s_mov_b32 s57, 0x7f800000
	v_fmac_f32_e32 v7, 0x3f317217, v2
	v_cmp_lt_f32_e64 vcc, |v2|, s57
	s_ashr_i32 s57, s56, 31
	s_nop 0
	v_cndmask_b32_e32 v2, v2, v7, vcc
	v_sub_f32_e32 v6, v2, v6
	v_fmac_f32_e32 v6, 0x3db504f3, v3
	v_mad_u64_u32 v[2:3], s[60:61], v4, 48, s[24:25]
	v_mov_b32_e32 v4, v3
	v_mad_u64_u32 v[4:5], s[60:61], v5, 48, v[4:5]
	v_mov_b32_e32 v3, v4
	v_lshl_add_u64 v[2:3], s[56:57], 2, v[2:3]
	global_store_dword v[2:3], v6, off
	s_branch .LBB0_242
